# expert GEMMs: unit-scale v_mfma_scale_f32_16x16x128_f8f6f4 replaced by the unscaled v_mfma_f32_16x16x128_f8f6f4 (same e4m3 operands, same numerics, one 8-byte instruction, no scale operand reads)
# baseline (speedup 1.0000x reference)
.LBB0_1087:
	v_add_u32_e32 v110, s67, v164
	ds_read_b128 v[168:171], v110
	ds_read_b128 v[172:175], v110 offset:1024
	ds_read_b128 v[176:179], v110 offset:2048
	ds_read_b128 v[180:183], v110 offset:3072
	v_add_u32_e32 v110, s68, v164
	ds_read_b128 v[184:187], v110
	ds_read_b128 v[188:191], v110 offset:1024
	ds_read_b128 v[192:195], v110 offset:2048
	ds_read_b128 v[196:199], v110 offset:3072
	s_add_u32 s1, s36, 0x80
	s_addc_u32 s42, s37, 0
	s_and_b64 s[40:41], s[38:39], exec
	s_cselect_b32 s41, s79, s42
	s_cselect_b32 s40, s78, s1
	s_cselect_b32 s43, s83, s72
	s_cselect_b32 s42, s82, s25
	ds_read_b128 v[200:203], v165
	ds_read_b128 v[204:207], v165 offset:1024
	ds_read_b128 v[208:211], v165 offset:2048
	ds_read_b128 v[212:215], v165 offset:3072
	ds_read_b128 v[216:219], v165 offset:4096
	ds_read_b128 v[220:223], v165 offset:5120
	ds_read_b128 v[226:229], v165 offset:6144
	ds_read_b128 v[230:233], v165 offset:7168
	s_add_i32 m0, s52, 0xc000
	s_nop 0
	global_load_lds_dwordx4 v160, s[36:37]
	v_mov_b32_e32 v110, v161
	s_add_i32 m0, s52, 0xe000
	s_nop 0
	global_load_lds_dwordx4 v110, s[36:37]
	s_waitcnt vmcnt(8)
	s_waitcnt lgkmcnt(0)
	s_barrier
	s_setprio 1
	s_waitcnt lgkmcnt(0)
	v_mfma_f32_16x16x128_f8f6f4 v[114:117], v[168:175], v[208:215], v[114:117]
	v_mfma_f32_16x16x128_f8f6f4 v[102:105], v[176:183], v[208:215], v[102:105]
	v_mfma_f32_16x16x128_f8f6f4 v[94:97], v[168:175], v[216:223], v[94:97]
	v_mfma_f32_16x16x128_f8f6f4 v[86:89], v[176:183], v[216:223], v[86:89]
	v_mfma_f32_16x16x128_f8f6f4 v[78:81], v[168:175], v[226:233], v[78:81]
	v_mfma_f32_16x16x128_f8f6f4 v[70:73], v[176:183], v[226:233], v[70:73]
	v_mfma_f32_16x16x128_f8f6f4 v[110:113], v[168:175], v[200:207], v[142:145]
	v_mfma_f32_16x16x128_f8f6f4 v[118:121], v[176:183], v[200:207], v[134:137]
	s_setprio 0
	s_setprio 1
	v_mfma_f32_16x16x128_f8f6f4 v[122:125], v[192:199], v[200:207], v[122:125]
	v_mfma_f32_16x16x128_f8f6f4 v[106:109], v[184:191], v[208:215], v[106:109]
	v_mfma_f32_16x16x128_f8f6f4 v[98:101], v[192:199], v[208:215], v[98:101]
	v_mfma_f32_16x16x128_f8f6f4 v[90:93], v[184:191], v[216:223], v[90:93]
	v_mfma_f32_16x16x128_f8f6f4 v[82:85], v[192:199], v[216:223], v[82:85]
	v_mfma_f32_16x16x128_f8f6f4 v[74:77], v[184:191], v[226:233], v[74:77]
	v_mfma_f32_16x16x128_f8f6f4 v[66:69], v[192:199], v[226:233], v[66:69]
	v_mfma_f32_16x16x128_f8f6f4 v[126:129], v[184:191], v[200:207], v[138:141]
	s_setprio 0
	s_barrier
	s_add_i32 s1, s67, s45
	ds_read_b128 v[134:137], v165 offset:16384
	s_nop 1
	ds_read_b128 v[138:141], v165 offset:17408
	ds_read_b128 v[200:203], v165 offset:18432
	ds_read_b128 v[204:207], v165 offset:19456
	ds_read_b128 v[208:211], v165 offset:20480
	ds_read_b128 v[212:215], v165 offset:21504
	ds_read_b128 v[216:219], v165 offset:22528
	ds_read_b128 v[220:223], v165 offset:23552
	s_mov_b32 m0, s1
	s_nop 0
	global_load_lds_dwordx4 v158, s[42:43]
	s_add_i32 m0, s1, 0x2000
	s_add_u32 s74, s42, 0x40000
	global_load_lds_dwordx4 v159, s[42:43]
	s_addc_u32 s75, s43, 0
	s_add_i32 s1, s68, s45
	s_mov_b32 m0, s1
	s_nop 0
	global_load_lds_dwordx4 v158, s[74:75]
	s_add_i32 m0, s1, 0x2000
	s_nop 0
	global_load_lds_dwordx4 v159, s[74:75]
	s_mov_b32 m0, s52
	s_nop 0
	global_load_lds_dwordx4 v133, s[40:41]
	v_mov_b32_e32 v142, v150
	s_mov_b32 m0, s53
	s_nop 0
	global_load_lds_dwordx4 v142, s[40:41]
	s_waitcnt vmcnt(8)
	s_waitcnt lgkmcnt(0)
	s_barrier
	s_setprio 1
	s_waitcnt lgkmcnt(0)
	v_mfma_f32_16x16x128_f8f6f4 v[62:65], v[168:175], v[134:141], v[62:65]
	v_mfma_f32_16x16x128_f8f6f4 v[54:57], v[176:183], v[134:141], v[54:57]
	v_mfma_f32_16x16x128_f8f6f4 v[46:49], v[168:175], v[200:207], v[46:49]
	v_mfma_f32_16x16x128_f8f6f4 v[38:41], v[176:183], v[200:207], v[38:41]
	v_mfma_f32_16x16x128_f8f6f4 v[30:33], v[168:175], v[208:215], v[30:33]
	v_mfma_f32_16x16x128_f8f6f4 v[22:25], v[176:183], v[208:215], v[22:25]
	v_mfma_f32_16x16x128_f8f6f4 v[14:17], v[168:175], v[216:223], v[14:17]
	v_mfma_f32_16x16x128_f8f6f4 v[6:9], v[176:183], v[216:223], v[6:9]
	s_setprio 0
	s_setprio 1
	v_mfma_f32_16x16x128_f8f6f4 v[58:61], v[184:191], v[134:141], v[58:61]
	v_mfma_f32_16x16x128_f8f6f4 v[50:53], v[192:199], v[134:141], v[50:53]
	v_mfma_f32_16x16x128_f8f6f4 v[42:45], v[184:191], v[200:207], v[42:45]
	v_mfma_f32_16x16x128_f8f6f4 v[34:37], v[192:199], v[200:207], v[34:37]
	v_mfma_f32_16x16x128_f8f6f4 v[26:29], v[184:191], v[208:215], v[26:29]
	v_mfma_f32_16x16x128_f8f6f4 v[18:21], v[192:199], v[208:215], v[18:21]
	v_mfma_f32_16x16x128_f8f6f4 v[10:13], v[184:191], v[216:223], v[10:13]
	v_mfma_f32_16x16x128_f8f6f4 v[2:5], v[192:199], v[216:223], v[2:5]
	s_setprio 0
	s_barrier
	s_add_i32 s1, 0, 0x18000
	v_add_u32_e32 v134, s1, v164
	s_add_i32 s73, 0, 0x1c000
	ds_read_b128 v[168:171], v134
	ds_read_b128 v[172:175], v134 offset:1024
	ds_read_b128 v[176:179], v134 offset:2048
	ds_read_b128 v[180:183], v134 offset:3072
	v_add_u32_e32 v134, s73, v164
	ds_read_b128 v[184:187], v134
	ds_read_b128 v[188:191], v134 offset:1024
	ds_read_b128 v[192:195], v134 offset:2048
	ds_read_b128 v[196:199], v134 offset:3072
	s_mov_b32 m0, s54
	ds_read_b128 v[200:203], v165 offset:32768
	ds_read_b128 v[204:207], v165 offset:33792
	ds_read_b128 v[208:211], v165 offset:34816
	ds_read_b128 v[212:215], v165 offset:35840
	ds_read_b128 v[216:219], v165 offset:36864
	ds_read_b128 v[220:223], v165 offset:37888
	ds_read_b128 v[226:229], v165 offset:38912
	ds_read_b128 v[230:233], v165 offset:39936
	s_nop 0
	global_load_lds_dwordx4 v151, s[40:41]
	v_mov_b32_e32 v134, v152
	s_mov_b32 m0, s55
	s_nop 0
	global_load_lds_dwordx4 v134, s[40:41]
	s_waitcnt vmcnt(8)
	s_waitcnt lgkmcnt(0)
	s_barrier
	s_setprio 1
	s_waitcnt lgkmcnt(0)
	v_mfma_f32_16x16x128_f8f6f4 v[142:145], v[168:175], v[200:207], v[110:113]
	v_mfma_f32_16x16x128_f8f6f4 v[134:137], v[176:183], v[200:207], v[118:121]
	v_mfma_f32_16x16x128_f8f6f4 v[114:117], v[168:175], v[208:215], v[114:117]
	v_mfma_f32_16x16x128_f8f6f4 v[102:105], v[176:183], v[208:215], v[102:105]
	v_mfma_f32_16x16x128_f8f6f4 v[94:97], v[168:175], v[216:223], v[94:97]
	v_mfma_f32_16x16x128_f8f6f4 v[86:89], v[176:183], v[216:223], v[86:89]
	v_mfma_f32_16x16x128_f8f6f4 v[78:81], v[168:175], v[226:233], v[78:81]
	v_mfma_f32_16x16x128_f8f6f4 v[70:73], v[176:183], v[226:233], v[70:73]
	s_setprio 0
	s_setprio 1
	v_mfma_f32_16x16x128_f8f6f4 v[138:141], v[184:191], v[200:207], v[126:129]
	v_mfma_f32_16x16x128_f8f6f4 v[122:125], v[192:199], v[200:207], v[122:125]
	v_mfma_f32_16x16x128_f8f6f4 v[106:109], v[184:191], v[208:215], v[106:109]
	v_mfma_f32_16x16x128_f8f6f4 v[98:101], v[192:199], v[208:215], v[98:101]
	v_mfma_f32_16x16x128_f8f6f4 v[90:93], v[184:191], v[216:223], v[90:93]
	v_mfma_f32_16x16x128_f8f6f4 v[82:85], v[192:199], v[216:223], v[82:85]
	v_mfma_f32_16x16x128_f8f6f4 v[74:77], v[184:191], v[226:233], v[74:77]
	v_mfma_f32_16x16x128_f8f6f4 v[66:69], v[192:199], v[226:233], v[66:69]
	s_setprio 0
	s_barrier
	v_mov_b32_e32 v146, v158
	ds_read_b128 v[200:203], v165 offset:49152
	ds_read_b128 v[204:207], v165 offset:50176
	ds_read_b128 v[208:211], v165 offset:51200
	ds_read_b128 v[212:215], v165 offset:52224
	ds_read_b128 v[216:219], v165 offset:53248
	ds_read_b128 v[220:223], v165 offset:54272
	ds_read_b128 v[226:229], v165 offset:55296
	ds_read_b128 v[230:233], v165 offset:56320
	s_add_i32 s1, s1, s45
	v_lshl_add_u64 v[110:111], s[42:43], 0, v[146:147]
	v_lshl_add_u64 v[110:111], v[110:111], 0, s[88:89]
	s_mov_b32 m0, s1
	v_mov_b32_e32 v146, v159
	global_load_lds_dwordx4 v[110:111], off
	s_add_i32 m0, s1, 0x2000
	v_lshl_add_u64 v[110:111], s[42:43], 0, v[146:147]
	v_lshl_add_u64 v[110:111], v[110:111], 0, s[88:89]
	s_add_u32 s42, s42, 0x40080
	global_load_lds_dwordx4 v[110:111], off
	s_addc_u32 s43, s43, 0
	s_add_i32 s1, s73, s45
	s_mov_b32 m0, s1
	v_mov_b32_e32 v146, v133
	global_load_lds_dwordx4 v158, s[42:43]
	v_mov_b32_e32 v110, v159
	s_add_i32 m0, s1, 0x2000
	s_nop 0
	global_load_lds_dwordx4 v110, s[42:43]
	s_mov_b32 m0, s59
	v_lshl_add_u64 v[110:111], s[40:41], 0, v[146:147]
	v_lshl_add_u64 v[110:111], v[110:111], 0, s[88:89]
	v_mov_b32_e32 v146, v150
	global_load_lds_dwordx4 v[110:111], off
	s_mov_b32 m0, s60
	v_lshl_add_u64 v[110:111], s[40:41], 0, v[146:147]
	v_lshl_add_u64 v[110:111], v[110:111], 0, s[88:89]
	global_load_lds_dwordx4 v[110:111], off
	s_waitcnt vmcnt(8)
	s_waitcnt lgkmcnt(0)
	s_barrier
	s_setprio 1
	s_waitcnt lgkmcnt(0)
	v_mfma_f32_16x16x128_f8f6f4 v[62:65], v[168:175], v[200:207], v[62:65]
	v_mfma_f32_16x16x128_f8f6f4 v[54:57], v[176:183], v[200:207], v[54:57]
	v_mfma_f32_16x16x128_f8f6f4 v[46:49], v[168:175], v[208:215], v[46:49]
	v_mfma_f32_16x16x128_f8f6f4 v[38:41], v[176:183], v[208:215], v[38:41]
	v_mfma_f32_16x16x128_f8f6f4 v[30:33], v[168:175], v[216:223], v[30:33]
	v_mfma_f32_16x16x128_f8f6f4 v[22:25], v[176:183], v[216:223], v[22:25]
	v_mfma_f32_16x16x128_f8f6f4 v[14:17], v[168:175], v[226:233], v[14:17]
	v_mfma_f32_16x16x128_f8f6f4 v[6:9], v[176:183], v[226:233], v[6:9]
	s_setprio 0
	s_setprio 1
	v_mfma_f32_16x16x128_f8f6f4 v[58:61], v[184:191], v[200:207], v[58:61]
	v_mfma_f32_16x16x128_f8f6f4 v[50:53], v[192:199], v[200:207], v[50:53]
	v_mfma_f32_16x16x128_f8f6f4 v[42:45], v[184:191], v[208:215], v[42:45]
	v_mfma_f32_16x16x128_f8f6f4 v[34:37], v[192:199], v[208:215], v[34:37]
	v_mfma_f32_16x16x128_f8f6f4 v[26:29], v[184:191], v[216:223], v[26:29]
	v_mfma_f32_16x16x128_f8f6f4 v[18:21], v[192:199], v[216:223], v[18:21]
	v_mfma_f32_16x16x128_f8f6f4 v[10:13], v[184:191], v[226:233], v[10:13]
	v_mfma_f32_16x16x128_f8f6f4 v[2:5], v[192:199], v[226:233], v[2:5]
	s_add_i32 s0, s0, 2
	s_add_u32 s25, s25, 0x100
	s_addc_u32 s72, s72, 0
	s_add_u32 s36, s36, 0x100
	s_addc_u32 s37, s37, 0
	s_setprio 0
	s_barrier
	s_andn2_b64 vcc, exec, s[38:39]
	s_cbranch_vccnz .LBB0_1084
	v_mov_b32_e32 v161, v152
	v_mov_b32_e32 v160, v151
	v_mov_b32_e32 v163, v150
	v_mov_b32_e32 v162, v133
	s_branch .LBB0_1084

.LBB0_1161:
	ds_read_b128 v[128:131], v157
	ds_read_b128 v[132:135], v157 offset:1024
	ds_read_b128 v[136:139], v157 offset:2048
	ds_read_b128 v[140:143], v157 offset:3072
	ds_read_b128 v[162:165], v158
	ds_read_b128 v[166:169], v158 offset:1024
	ds_read_b128 v[170:173], v158 offset:2048
	ds_read_b128 v[174:177], v158 offset:3072
	s_add_u32 s23, s34, 0x80
	s_addc_u32 s33, s35, 0
	s_cmp_eq_u32 s21, 12
	s_cselect_b32 s37, s25, s33
	s_cselect_b32 s36, s24, s23
	s_cselect_b32 s39, s5, s1
	s_cselect_b32 s38, s4, s0
	ds_read_b128 v[178:181], v159
	ds_read_b128 v[182:185], v159 offset:1024
	ds_read_b128 v[186:189], v159 offset:2048
	ds_read_b128 v[190:193], v159 offset:3072
	ds_read_b128 v[194:197], v159 offset:4096
	ds_read_b128 v[198:201], v159 offset:5120
	ds_read_b128 v[202:205], v159 offset:6144
	ds_read_b128 v[206:209], v159 offset:7168
	s_add_i32 m0, s31, 0xc000
	s_nop 0
	global_load_lds_dwordx4 v153, s[34:35]
	s_add_i32 m0, s31, 0xe000
	s_nop 0
	global_load_lds_dwordx4 v155, s[34:35]
	s_waitcnt vmcnt(8)
	s_waitcnt lgkmcnt(0)
	s_barrier
	s_setprio 1
	s_waitcnt lgkmcnt(0)
	v_mfma_f32_16x16x128_f8f6f4 v[124:127], v[128:135], v[178:185], v[124:127]
	v_mfma_f32_16x16x128_f8f6f4 v[120:123], v[136:143], v[178:185], v[120:123]
	v_mfma_f32_16x16x128_f8f6f4 v[116:119], v[128:135], v[186:193], v[116:119]
	v_mfma_f32_16x16x128_f8f6f4 v[112:115], v[136:143], v[186:193], v[112:115]
	v_mfma_f32_16x16x128_f8f6f4 v[210:213], v[128:135], v[194:201], v[92:95]
	v_mfma_f32_16x16x128_f8f6f4 v[214:217], v[136:143], v[194:201], v[88:91]
	v_mfma_f32_16x16x128_f8f6f4 v[218:221], v[128:135], v[202:209], v[84:87]
	v_mfma_f32_16x16x128_f8f6f4 v[226:229], v[136:143], v[202:209], v[80:83]
	s_setprio 0
	s_setprio 1
	v_mfma_f32_16x16x128_f8f6f4 v[108:111], v[162:169], v[178:185], v[108:111]
	v_mfma_f32_16x16x128_f8f6f4 v[104:107], v[170:177], v[178:185], v[104:107]
	v_mfma_f32_16x16x128_f8f6f4 v[100:103], v[162:169], v[186:193], v[100:103]
	v_mfma_f32_16x16x128_f8f6f4 v[96:99], v[170:177], v[186:193], v[96:99]
	v_mfma_f32_16x16x128_f8f6f4 v[230:233], v[162:169], v[194:201], v[76:79]
	v_mfma_f32_16x16x128_f8f6f4 v[194:197], v[170:177], v[194:201], v[72:75]
	v_mfma_f32_16x16x128_f8f6f4 v[198:201], v[162:169], v[202:209], v[68:71]
	v_mfma_f32_16x16x128_f8f6f4 v[202:205], v[170:177], v[202:209], v[64:67]
	s_setprio 0
	s_barrier
	s_add_i32 s23, s57, s43
	s_nop 2
	ds_read_b128 v[64:67], v159 offset:16384
	ds_read_b128 v[68:71], v159 offset:17408
	ds_read_b128 v[72:75], v159 offset:18432
	ds_read_b128 v[76:79], v159 offset:19456
	ds_read_b128 v[80:83], v159 offset:20480
	ds_read_b128 v[84:87], v159 offset:21504
	ds_read_b128 v[88:91], v159 offset:22528
	ds_read_b128 v[92:95], v159 offset:23552
	s_mov_b32 m0, s23
	s_nop 0
	global_load_lds_dwordx4 v150, s[38:39]
	s_add_i32 m0, s23, 0x2000
	s_add_u32 s62, s38, 0x40000
	global_load_lds_dwordx4 v151, s[38:39]
	s_addc_u32 s63, s39, 0
	s_add_i32 s23, s58, s43
	s_mov_b32 m0, s23
	s_nop 0
	global_load_lds_dwordx4 v150, s[62:63]
	s_add_i32 m0, s23, 0x2000
	s_nop 0
	global_load_lds_dwordx4 v151, s[62:63]
	s_mov_b32 m0, s31
	s_nop 0
	global_load_lds_dwordx4 v152, s[36:37]
	s_mov_b32 m0, s49
	s_nop 0
	global_load_lds_dwordx4 v154, s[36:37]
	s_waitcnt vmcnt(8)
	s_waitcnt lgkmcnt(0)
	s_barrier
	s_setprio 1
	s_waitcnt lgkmcnt(0)
	v_mfma_f32_16x16x128_f8f6f4 v[60:63], v[128:135], v[64:71], v[60:63]
	v_mfma_f32_16x16x128_f8f6f4 v[56:59], v[136:143], v[64:71], v[56:59]
	v_mfma_f32_16x16x128_f8f6f4 v[52:55], v[128:135], v[72:79], v[52:55]
	v_mfma_f32_16x16x128_f8f6f4 v[48:51], v[136:143], v[72:79], v[48:51]
	v_mfma_f32_16x16x128_f8f6f4 v[28:31], v[128:135], v[80:87], v[28:31]
	v_mfma_f32_16x16x128_f8f6f4 v[24:27], v[136:143], v[80:87], v[24:27]
	v_mfma_f32_16x16x128_f8f6f4 v[20:23], v[128:135], v[88:95], v[20:23]
	v_mfma_f32_16x16x128_f8f6f4 v[16:19], v[136:143], v[88:95], v[16:19]
	s_setprio 0
	s_setprio 1
	v_mfma_f32_16x16x128_f8f6f4 v[44:47], v[162:169], v[64:71], v[44:47]
	v_mfma_f32_16x16x128_f8f6f4 v[40:43], v[170:177], v[64:71], v[40:43]
	v_mfma_f32_16x16x128_f8f6f4 v[36:39], v[162:169], v[72:79], v[36:39]
	v_mfma_f32_16x16x128_f8f6f4 v[32:35], v[170:177], v[72:79], v[32:35]
	v_mfma_f32_16x16x128_f8f6f4 v[12:15], v[162:169], v[80:87], v[12:15]
	v_mfma_f32_16x16x128_f8f6f4 v[8:11], v[170:177], v[80:87], v[8:11]
	v_mfma_f32_16x16x128_f8f6f4 v[4:7], v[162:169], v[88:95], v[4:7]
	v_mfma_f32_16x16x128_f8f6f4 v[0:3], v[170:177], v[88:95], v[0:3]
	s_setprio 0
	s_barrier
	s_add_i32 s23, 0, 0x18000
	v_add_u32_e32 v64, s23, v156
	s_add_i32 s33, 0, 0x1c000
	ds_read_b128 v[128:131], v64
	ds_read_b128 v[132:135], v64 offset:1024
	ds_read_b128 v[136:139], v64 offset:2048
	ds_read_b128 v[140:143], v64 offset:3072
	v_add_u32_e32 v64, s33, v156
	ds_read_b128 v[162:165], v64
	ds_read_b128 v[166:169], v64 offset:1024
	ds_read_b128 v[170:173], v64 offset:2048
	ds_read_b128 v[174:177], v64 offset:3072
	s_mov_b32 m0, s50
	ds_read_b128 v[64:67], v159 offset:32768
	ds_read_b128 v[68:71], v159 offset:33792
	ds_read_b128 v[72:75], v159 offset:34816
	ds_read_b128 v[76:79], v159 offset:35840
	ds_read_b128 v[178:181], v159 offset:36864
	ds_read_b128 v[182:185], v159 offset:37888
	ds_read_b128 v[186:189], v159 offset:38912
	ds_read_b128 v[190:193], v159 offset:39936
	s_nop 0
	global_load_lds_dwordx4 v153, s[36:37]
	v_mov_b32_e32 v80, v155
	s_mov_b32 m0, s51
	s_nop 0
	global_load_lds_dwordx4 v80, s[36:37]
	s_waitcnt vmcnt(8)
	s_waitcnt lgkmcnt(0)
	s_barrier
	s_setprio 1
	s_waitcnt lgkmcnt(0)
	v_mfma_f32_16x16x128_f8f6f4 v[124:127], v[128:135], v[64:71], v[124:127]
	v_mfma_f32_16x16x128_f8f6f4 v[120:123], v[136:143], v[64:71], v[120:123]
	v_mfma_f32_16x16x128_f8f6f4 v[116:119], v[128:135], v[72:79], v[116:119]
	v_mfma_f32_16x16x128_f8f6f4 v[112:115], v[136:143], v[72:79], v[112:115]
	v_mfma_f32_16x16x128_f8f6f4 v[92:95], v[128:135], v[178:185], v[210:213]
	v_mfma_f32_16x16x128_f8f6f4 v[88:91], v[136:143], v[178:185], v[214:217]
	v_mfma_f32_16x16x128_f8f6f4 v[84:87], v[128:135], v[186:193], v[218:221]
	v_mfma_f32_16x16x128_f8f6f4 v[80:83], v[136:143], v[186:193], v[226:229]
	s_setprio 0
	s_setprio 1
	v_mfma_f32_16x16x128_f8f6f4 v[108:111], v[162:169], v[64:71], v[108:111]
	v_mfma_f32_16x16x128_f8f6f4 v[104:107], v[170:177], v[64:71], v[104:107]
	v_mfma_f32_16x16x128_f8f6f4 v[100:103], v[162:169], v[72:79], v[100:103]
	v_mfma_f32_16x16x128_f8f6f4 v[96:99], v[170:177], v[72:79], v[96:99]
	v_mfma_f32_16x16x128_f8f6f4 v[76:79], v[162:169], v[178:185], v[230:233]
	v_mfma_f32_16x16x128_f8f6f4 v[72:75], v[170:177], v[178:185], v[194:197]
	v_mfma_f32_16x16x128_f8f6f4 v[68:71], v[162:169], v[186:193], v[198:201]
	v_mfma_f32_16x16x128_f8f6f4 v[64:67], v[170:177], v[186:193], v[202:205]
	s_setprio 0
	s_barrier
	v_mov_b32_e32 v144, v150
	ds_read_b128 v[178:181], v159 offset:49152
	ds_read_b128 v[182:185], v159 offset:50176
	ds_read_b128 v[186:189], v159 offset:51200
	ds_read_b128 v[190:193], v159 offset:52224
	ds_read_b128 v[194:197], v159 offset:53248
	ds_read_b128 v[198:201], v159 offset:54272
	ds_read_b128 v[202:205], v159 offset:55296
	ds_read_b128 v[206:209], v159 offset:56320
	s_add_i32 s23, s23, s43
	v_lshl_add_u64 v[148:149], s[38:39], 0, v[144:145]
	v_lshl_add_u64 v[148:149], v[148:149], 0, s[14:15]
	s_mov_b32 m0, s23
	v_mov_b32_e32 v144, v151
	global_load_lds_dwordx4 v[148:149], off
	s_add_i32 m0, s23, 0x2000
	s_nop 0
	v_lshl_add_u64 v[148:149], s[38:39], 0, v[144:145]
	s_add_u32 s38, s38, 0x40080
	v_lshl_add_u64 v[148:149], v[148:149], 0, s[14:15]
	s_addc_u32 s39, s39, 0
	s_add_i32 s23, s33, s43
	global_load_lds_dwordx4 v[148:149], off
	s_mov_b32 m0, s23
	s_nop 0
	global_load_lds_dwordx4 v150, s[38:39]
	s_add_i32 m0, s23, 0x2000
	s_nop 0
	global_load_lds_dwordx4 v151, s[38:39]
	v_mov_b32_e32 v144, v152
	s_mov_b32 m0, s52
	v_lshl_add_u64 v[148:149], s[36:37], 0, v[144:145]
	v_lshl_add_u64 v[148:149], v[148:149], 0, s[14:15]
	v_mov_b32_e32 v144, v154
	global_load_lds_dwordx4 v[148:149], off
	s_mov_b32 m0, s53
	v_lshl_add_u64 v[148:149], s[36:37], 0, v[144:145]
	v_lshl_add_u64 v[148:149], v[148:149], 0, s[14:15]
	global_load_lds_dwordx4 v[148:149], off
	s_waitcnt vmcnt(8)
	s_waitcnt lgkmcnt(0)
	s_barrier
	s_setprio 1
	s_waitcnt lgkmcnt(0)
	v_mfma_f32_16x16x128_f8f6f4 v[60:63], v[128:135], v[178:185], v[60:63]
	v_mfma_f32_16x16x128_f8f6f4 v[56:59], v[136:143], v[178:185], v[56:59]
	v_mfma_f32_16x16x128_f8f6f4 v[52:55], v[128:135], v[186:193], v[52:55]
	v_mfma_f32_16x16x128_f8f6f4 v[48:51], v[136:143], v[186:193], v[48:51]
	v_mfma_f32_16x16x128_f8f6f4 v[28:31], v[128:135], v[194:201], v[28:31]
	v_mfma_f32_16x16x128_f8f6f4 v[24:27], v[136:143], v[194:201], v[24:27]
	v_mfma_f32_16x16x128_f8f6f4 v[20:23], v[128:135], v[202:209], v[20:23]
	v_mfma_f32_16x16x128_f8f6f4 v[16:19], v[136:143], v[202:209], v[16:19]
	s_setprio 0
	s_setprio 1
	v_mfma_f32_16x16x128_f8f6f4 v[44:47], v[162:169], v[178:185], v[44:47]
	v_mfma_f32_16x16x128_f8f6f4 v[40:43], v[170:177], v[178:185], v[40:43]
	v_mfma_f32_16x16x128_f8f6f4 v[36:39], v[162:169], v[186:193], v[36:39]
	v_mfma_f32_16x16x128_f8f6f4 v[32:35], v[170:177], v[186:193], v[32:35]
	v_mfma_f32_16x16x128_f8f6f4 v[12:15], v[162:169], v[194:201], v[12:15]
	v_mfma_f32_16x16x128_f8f6f4 v[8:11], v[170:177], v[194:201], v[8:11]
	v_mfma_f32_16x16x128_f8f6f4 v[4:7], v[162:169], v[202:209], v[4:7]
	v_mfma_f32_16x16x128_f8f6f4 v[0:3], v[170:177], v[202:209], v[0:3]
	s_add_i32 s21, s21, 2
	s_add_u32 s0, s0, 0x100
	s_addc_u32 s1, s1, 0
	s_add_u32 s34, s34, 0x100
	s_addc_u32 s35, s35, 0
	s_cmp_gt_u32 s21, 13
	s_setprio 0
	s_barrier
	s_cbranch_scc0 .LBB0_1161
	s_and_b64 vcc, exec, s[16:17]
	s_cbranch_vccz .LBB0_1164
	s_barrier
